# DeltaNet prep conv stage: q/k row-norm partial sums reduced with quad_perm DPP adds instead of two ds_bpermute rounds (bit-identical), on top of the DPP gate cumsum build
# baseline (speedup 1.0000x reference)
; __device__ __forceinline__ float lo16(unsigned u) { return __uint_as_float(u << 16); }
; __device__ __forceinline__ float hi16(unsigned u) { return __uint_as_float(u & 0xffff0000u); }
; __device__ void phase_gdn_prep(const Params& p, int l, char* smem, int vb, int nvb, int pend, int oz) {
;     ...
;         {
;             const int t = tid >> 2, qt = tid & 3;
; #pragma unroll
;             for (int which = 0; which < 3; ++which) {
;                 float a[16];
; #pragma unroll
;                 for (int i = 0; i < 16; ++i) a[i] = 0.f;
; #pragma unroll
;                 for (int j = 0; j < 4; ++j) {
;                     const u32x4 x0 = *(const u32x4*)(raw + (t + j) * 192 + which * 64 + qt * 16);
;                     const u32x4 x1 = *(const u32x4*)(raw + (t + j) * 192 + which * 64 + qt * 16 + 8);
;                     const float* cwp = cwl + j * 192 + which * 64 + qt * 16;
; #pragma unroll
;                     for (int w = 0; w < 4; ++w) {
;                         a[2 * w] += cwp[2 * w] * lo16(x0[w]);
;                         a[2 * w + 1] += cwp[2 * w + 1] * hi16(x0[w]);
;                         a[8 + 2 * w] += cwp[8 + 2 * w] * lo16(x1[w]);
;                         a[8 + 2 * w + 1] += cwp[8 + 2 * w + 1] * hi16(x1[w]);
;                     }
;                 }
.LBB0_523:
	s_or_b64 exec, exec, s[0:1]
	v_lshlrev_b32_e32 v2, 5, v8
	v_and_b32_e32 v2, 0x60, v2
	v_lshrrev_b32_e32 v63, 2, v9
	v_add_u32_e32 v64, s81, v2
	s_movk_i32 s0, 0x180
	v_add_u32_e32 v61, v64, v2
	v_mad_u32_u24 v62, v63, s0, v64
	s_waitcnt lgkmcnt(0)
	s_barrier
	ds_read_b128 v[16:19], v62
	ds_read_b128 v[26:29], v62 offset:16
	ds_read_b128 v[12:15], v62 offset:384
	ds_read_b128 v[30:33], v62 offset:400
	ds_read_b128 v[8:11], v62 offset:768
	ds_read_b128 v[34:37], v62 offset:784
	ds_read_b128 v[4:7], v62 offset:1152
	ds_read_b128 v[38:41], v62 offset:1168
	ds_read_b128 v[42:45], v61 offset:53408
	ds_read_b128 v[20:23], v61 offset:53424
	v_and_b32_e32 v2, 64, v236
	ds_read_b128 v[46:49], v61 offset:54192
	ds_read_b128 v[50:53], v61 offset:54176
	v_xor_b32_e32 v24, 1, v236
	v_add_u32_e32 v65, 64, v2
	v_cmp_lt_i32_e32 vcc, v24, v65
	s_waitcnt lgkmcnt(10)
	v_and_b32_e32 v25, 0xffff0000, v29
	s_waitcnt lgkmcnt(6)
	v_lshlrev_b32_e32 v58, 16, v37
	v_cndmask_b32_e32 v66, v236, v24, vcc
	v_lshlrev_b32_e32 v24, 16, v29
	s_waitcnt lgkmcnt(2)
	v_pk_fma_f32 v[22:23], v[22:23], v[24:25], 0 op_sel_hi:[1,1,0]
	v_lshlrev_b32_e32 v24, 16, v33
	v_and_b32_e32 v25, 0xffff0000, v33
	s_waitcnt lgkmcnt(1)
	v_pk_fma_f32 v[48:49], v[48:49], v[24:25], v[22:23]
	ds_read_b128 v[22:25], v61 offset:54960
	ds_read_b128 v[54:57], v61 offset:55728
	ds_read_b128 v[68:71], v61 offset:54944
	v_and_b32_e32 v59, 0xffff0000, v37
	ds_read_b128 v[72:75], v61 offset:55712
	v_lshlrev_b32_e32 v66, 2, v66
	s_waitcnt lgkmcnt(3)
	v_pk_fma_f32 v[24:25], v[24:25], v[58:59], v[48:49]
	v_lshlrev_b32_e32 v48, 16, v41
	v_and_b32_e32 v49, 0xffff0000, v41
	s_waitcnt lgkmcnt(2)
	v_pk_fma_f32 v[24:25], v[56:57], v[48:49], v[24:25]
	v_lshlrev_b32_e32 v48, 16, v28
	v_mul_f32_e32 v29, 0xbfb8aa3b, v24
	v_exp_f32_e32 v29, v29
	v_and_b32_e32 v49, 0xffff0000, v28
	v_pk_fma_f32 v[20:21], v[20:21], v[48:49], 0 op_sel_hi:[1,1,0]
	v_lshlrev_b32_e32 v28, 16, v32
	v_add_f32_e32 v29, 1.0, v29
	v_rcp_f32_e32 v58, v29
	v_and_b32_e32 v29, 0xffff0000, v32
	v_pk_fma_f32 v[20:21], v[46:47], v[28:29], v[20:21]
	v_lshlrev_b32_e32 v28, 16, v36
	v_and_b32_e32 v29, 0xffff0000, v36
	v_pk_fma_f32 v[20:21], v[22:23], v[28:29], v[20:21]
	v_lshlrev_b32_e32 v22, 16, v40
	v_and_b32_e32 v23, 0xffff0000, v40
	v_pk_fma_f32 v[22:23], v[54:55], v[22:23], v[20:21]
	v_mul_f32_e32 v33, 0xbfb8aa3b, v25
	v_mul_f32_e32 v20, 0xbfb8aa3b, v22
	v_exp_f32_e32 v20, v20
	v_mul_f32_e32 v21, 0xbfb8aa3b, v23
	v_exp_f32_e32 v21, v21
	v_exp_f32_e32 v33, v33
	v_add_f32_e32 v20, 1.0, v20
	v_rcp_f32_e32 v28, v20
	v_add_f32_e32 v20, 1.0, v21
	v_rcp_f32_e32 v29, v20
	v_add_f32_e32 v33, 1.0, v33
	v_rcp_f32_e32 v59, v33
	v_lshlrev_b32_e32 v32, 16, v31
	v_pk_mul_f32 v[22:23], v[22:23], v[28:29]
	v_lshlrev_b32_e32 v28, 16, v27
	v_and_b32_e32 v29, 0xffff0000, v27
	v_pk_fma_f32 v[28:29], v[44:45], v[28:29], 0 op_sel_hi:[1,1,0]
	v_and_b32_e32 v33, 0xffff0000, v31
	v_pk_fma_f32 v[28:29], v[52:53], v[32:33], v[28:29]
	v_lshlrev_b32_e32 v32, 16, v35
	v_and_b32_e32 v33, 0xffff0000, v35
	s_waitcnt lgkmcnt(1)
	v_pk_fma_f32 v[28:29], v[70:71], v[32:33], v[28:29]
	v_lshlrev_b32_e32 v32, 16, v39
	v_and_b32_e32 v33, 0xffff0000, v39
	s_waitcnt lgkmcnt(0)
	v_pk_fma_f32 v[32:33], v[74:75], v[32:33], v[28:29]
	v_lshlrev_b32_e32 v40, 16, v26
	v_mul_f32_e32 v27, 0xbfb8aa3b, v32
	v_exp_f32_e32 v27, v27
	v_mul_f32_e32 v28, 0xbfb8aa3b, v33
	v_exp_f32_e32 v31, v28
	v_and_b32_e32 v41, 0xffff0000, v26
	v_add_f32_e32 v27, 1.0, v27
	v_rcp_f32_e32 v36, v27
	v_add_f32_e32 v27, 1.0, v31
	v_rcp_f32_e32 v37, v27
	v_pk_fma_f32 v[26:27], v[42:43], v[40:41], 0 op_sel_hi:[1,1,0]
	v_lshlrev_b32_e32 v40, 16, v30
	v_and_b32_e32 v41, 0xffff0000, v30
	v_pk_fma_f32 v[26:27], v[50:51], v[40:41], v[26:27]
	v_lshlrev_b32_e32 v30, 16, v34
	v_and_b32_e32 v31, 0xffff0000, v34
	v_pk_fma_f32 v[26:27], v[68:69], v[30:31], v[26:27]
	v_lshlrev_b32_e32 v30, 16, v38
	v_and_b32_e32 v31, 0xffff0000, v38
	v_pk_fma_f32 v[30:31], v[72:73], v[30:31], v[26:27]
	ds_read_b128 v[46:49], v61 offset:53376
	ds_read_b128 v[54:57], v61 offset:53392
	v_mul_f32_e32 v26, 0xbfb8aa3b, v30
	v_exp_f32_e32 v34, v26
	v_mul_f32_e32 v26, 0xbfb8aa3b, v31
	v_exp_f32_e32 v35, v26
	ds_read_b128 v[38:41], v61 offset:54160
	ds_read_b128 v[42:45], v61 offset:54144
	ds_read_b128 v[50:53], v61 offset:54928
	v_pk_mul_f32 v[26:27], v[32:33], v[36:37]
	v_add_f32_e32 v32, 1.0, v34
	v_add_f32_e32 v33, 1.0, v35
	v_lshlrev_b32_e32 v34, 16, v19
	v_and_b32_e32 v35, 0xffff0000, v19
	v_pk_mul_f32 v[20:21], v[24:25], v[58:59]
	s_waitcnt lgkmcnt(3)
	v_pk_fma_f32 v[34:35], v[56:57], v[34:35], 0 op_sel_hi:[1,1,0]
	ds_read_b128 v[56:59], v61 offset:55696
	ds_read_b128 v[68:71], v61 offset:54912
	v_lshlrev_b32_e32 v36, 16, v15
	v_and_b32_e32 v37, 0xffff0000, v15
	s_waitcnt lgkmcnt(4)
	v_pk_fma_f32 v[34:35], v[40:41], v[36:37], v[34:35]
	v_lshlrev_b32_e32 v36, 16, v11
	v_and_b32_e32 v37, 0xffff0000, v11
	s_waitcnt lgkmcnt(2)
	v_pk_fma_f32 v[34:35], v[52:53], v[36:37], v[34:35]
	v_lshlrev_b32_e32 v36, 16, v7
	v_and_b32_e32 v37, 0xffff0000, v7
	s_waitcnt lgkmcnt(1)
; __device__ __forceinline__ float siluf_(float x) { return x * __builtin_amdgcn_rcpf(1.f + fexp(-x)); }
; __device__ __forceinline__ float lo16(unsigned u) { return __uint_as_float(u << 16); }
; __device__ __forceinline__ float hi16(unsigned u) { return __uint_as_float(u & 0xffff0000u); }
; __device__ void phase_gdn_prep(const Params& p, int l, char* smem, int vb, int nvb, int pend, int oz) {
;     ...
;                 for (int j = 0; j < 4; ++j) {
;                     const u32x4 x0 = *(const u32x4*)(raw + (t + j) * 192 + which * 64 + qt * 16);
;                     const u32x4 x1 = *(const u32x4*)(raw + (t + j) * 192 + which * 64 + qt * 16 + 8);
;                     const float* cwp = cwl + j * 192 + which * 64 + qt * 16;
; #pragma unroll
;                     for (int w = 0; w < 4; ++w) {
;                         a[2 * w] += cwp[2 * w] * lo16(x0[w]);
;                         a[2 * w + 1] += cwp[2 * w + 1] * hi16(x0[w]);
;                         a[8 + 2 * w] += cwp[8 + 2 * w] * lo16(x1[w]);
;                         a[8 + 2 * w + 1] += cwp[8 + 2 * w + 1] * hi16(x1[w]);
;                     }
;                 }
;                 float ss = 0.f;
; #pragma unroll
;                 for (int i = 0; i < 16; ++i) {
;                     a[i] = siluf_(a[i]);
;                     ss += a[i] * a[i];
;                 }
	v_pk_fma_f32 v[40:41], v[58:59], v[36:37], v[34:35]
	v_rcp_f32_e32 v32, v32
	v_mul_f32_e32 v7, 0xbfb8aa3b, v40
	v_exp_f32_e32 v7, v7
	v_mul_f32_e32 v11, 0xbfb8aa3b, v41
	v_exp_f32_e32 v11, v11
	v_rcp_f32_e32 v33, v33
	v_add_f32_e32 v7, 1.0, v7
	v_rcp_f32_e32 v52, v7
	v_add_f32_e32 v7, 1.0, v11
	v_rcp_f32_e32 v53, v7
	v_pk_mul_f32 v[30:31], v[30:31], v[32:33]
	ds_read_b128 v[72:75], v61 offset:55680
	v_pk_mul_f32 v[36:37], v[30:31], v[30:31]
	v_pk_mul_f32 v[32:33], v[40:41], v[52:53]
	v_lshlrev_b32_e32 v40, 16, v18
	v_and_b32_e32 v41, 0xffff0000, v18
	v_pk_fma_f32 v[18:19], v[54:55], v[40:41], 0 op_sel_hi:[1,1,0]
	v_lshlrev_b32_e32 v40, 16, v14
	v_and_b32_e32 v41, 0xffff0000, v14
	v_pk_fma_f32 v[14:15], v[38:39], v[40:41], v[18:19]
	v_lshlrev_b32_e32 v18, 16, v10
	v_and_b32_e32 v19, 0xffff0000, v10
	v_pk_fma_f32 v[10:11], v[50:51], v[18:19], v[14:15]
	v_lshlrev_b32_e32 v14, 16, v6
	v_and_b32_e32 v15, 0xffff0000, v6
	v_pk_fma_f32 v[40:41], v[56:57], v[14:15], v[10:11]
	v_lshlrev_b32_e32 v10, 16, v13
	v_mul_f32_e32 v6, 0xbfb8aa3b, v40
	v_exp_f32_e32 v6, v6
	v_mul_f32_e32 v7, 0xbfb8aa3b, v41
	v_exp_f32_e32 v7, v7
	v_and_b32_e32 v11, 0xffff0000, v13
	v_add_f32_e32 v6, 1.0, v6
	v_rcp_f32_e32 v54, v6
	v_add_f32_e32 v14, 1.0, v7
	v_lshlrev_b32_e32 v6, 16, v17
	v_and_b32_e32 v7, 0xffff0000, v17
	v_pk_fma_f32 v[6:7], v[48:49], v[6:7], 0 op_sel_hi:[1,1,0]
	v_rcp_f32_e32 v55, v14
	v_pk_fma_f32 v[6:7], v[44:45], v[10:11], v[6:7]
	v_lshlrev_b32_e32 v10, 16, v9
	v_and_b32_e32 v11, 0xffff0000, v9
	s_waitcnt lgkmcnt(1)
	v_pk_fma_f32 v[6:7], v[70:71], v[10:11], v[6:7]
	v_lshlrev_b32_e32 v10, 16, v5
	v_and_b32_e32 v11, 0xffff0000, v5
	s_waitcnt lgkmcnt(0)
	v_pk_fma_f32 v[48:49], v[74:75], v[10:11], v[6:7]
	v_and_b32_e32 v7, 0xffff0000, v16
	v_mul_f32_e32 v5, 0xbfb8aa3b, v48
	v_exp_f32_e32 v5, v5
	v_mul_f32_e32 v6, 0xbfb8aa3b, v49
	v_exp_f32_e32 v6, v6
	v_lshlrev_b32_e32 v10, 16, v12
	v_add_f32_e32 v5, 1.0, v5
	v_rcp_f32_e32 v132, v5
	v_add_f32_e32 v5, 1.0, v6
	v_lshlrev_b32_e32 v6, 16, v16
	v_pk_fma_f32 v[6:7], v[46:47], v[6:7], 0 op_sel_hi:[1,1,0]
	v_and_b32_e32 v11, 0xffff0000, v12
	v_pk_fma_f32 v[6:7], v[42:43], v[10:11], v[6:7]
	v_lshlrev_b32_e32 v10, 16, v8
	v_and_b32_e32 v11, 0xffff0000, v8
	v_pk_fma_f32 v[6:7], v[68:69], v[10:11], v[6:7]
	v_lshlrev_b32_e32 v8, 16, v4
	v_and_b32_e32 v9, 0xffff0000, v4
	v_pk_fma_f32 v[134:135], v[72:73], v[8:9], v[6:7]
	v_rcp_f32_e32 v133, v5
	v_mul_f32_e32 v4, 0xbfb8aa3b, v134
	v_exp_f32_e32 v4, v4
	v_mul_f32_e32 v6, 0xbfb8aa3b, v135
	v_exp_f32_e32 v6, v6
	v_pk_mul_f32 v[38:39], v[32:33], v[32:33]
	v_add_f32_e32 v4, 1.0, v4
	v_rcp_f32_e32 v136, v4
	v_add_f32_e32 v67, 1.0, v6
	ds_read_b128 v[16:19], v62 offset:128
	ds_read_b128 v[50:53], v62 offset:144
	ds_read_b128 v[12:15], v62 offset:512
	ds_read_b128 v[56:59], v62 offset:528
	ds_read_b128 v[8:11], v62 offset:896
	ds_read_b128 v[68:71], v62 offset:912
	ds_read_b128 v[4:7], v62 offset:1280
	ds_read_b128 v[72:75], v62 offset:1296
	ds_read_b128 v[42:45], v61 offset:53680
	ds_read_b128 v[76:79], v61 offset:54448
	ds_read_b128 v[80:83], v61 offset:53664
	ds_read_b128 v[84:87], v61 offset:54432
	ds_read_b128 v[88:91], v61 offset:55216
	s_waitcnt lgkmcnt(11)
	v_lshlrev_b32_e32 v46, 16, v53
	v_and_b32_e32 v47, 0xffff0000, v53
	ds_read_b128 v[92:95], v61 offset:55984
	ds_read_b128 v[96:99], v61 offset:55200
	s_waitcnt lgkmcnt(6)
	v_pk_fma_f32 v[44:45], v[44:45], v[46:47], 0 op_sel_hi:[1,1,0]
	v_lshlrev_b32_e32 v46, 16, v59
	v_and_b32_e32 v47, 0xffff0000, v59
	s_waitcnt lgkmcnt(5)
	v_pk_fma_f32 v[44:45], v[78:79], v[46:47], v[44:45]
	v_lshlrev_b32_e32 v46, 16, v71
	v_and_b32_e32 v47, 0xffff0000, v71
	s_waitcnt lgkmcnt(2)
	v_pk_fma_f32 v[44:45], v[90:91], v[46:47], v[44:45]
	v_lshlrev_b32_e32 v46, 16, v75
	v_and_b32_e32 v47, 0xffff0000, v75
	s_waitcnt lgkmcnt(1)
	v_pk_fma_f32 v[78:79], v[94:95], v[46:47], v[44:45]
	v_and_b32_e32 v53, 0xffff0000, v58
	v_mul_f32_e32 v44, 0xbfb8aa3b, v78
	v_exp_f32_e32 v44, v44
	v_mul_f32_e32 v45, 0xbfb8aa3b, v79
	v_exp_f32_e32 v45, v45
	ds_read_b128 v[100:103], v61 offset:55968
	v_add_f32_e32 v44, 1.0, v44
	v_rcp_f32_e32 v90, v44
	v_add_f32_e32 v44, 1.0, v45
	v_rcp_f32_e32 v91, v44
	v_pk_mul_f32 v[44:45], v[40:41], v[54:55]
	v_lshlrev_b32_e32 v54, 16, v52
	v_and_b32_e32 v55, 0xffff0000, v52
	v_pk_fma_f32 v[42:43], v[42:43], v[54:55], 0 op_sel_hi:[1,1,0]
	v_lshlrev_b32_e32 v52, 16, v58
	v_pk_fma_f32 v[42:43], v[76:77], v[52:53], v[42:43]
	v_lshlrev_b32_e32 v52, 16, v70
	v_and_b32_e32 v53, 0xffff0000, v70
	v_pk_fma_f32 v[42:43], v[88:89], v[52:53], v[42:43]
	v_lshlrev_b32_e32 v52, 16, v74
	v_and_b32_e32 v53, 0xffff0000, v74
	v_pk_fma_f32 v[42:43], v[92:93], v[52:53], v[42:43]
	v_lshlrev_b32_e32 v58, 16, v51
	v_and_b32_e32 v59, 0xffff0000, v51
	v_mul_f32_e32 v52, 0xbfb8aa3b, v42
	v_mul_f32_e32 v53, 0xbfb8aa3b, v43
	v_pk_fma_f32 v[58:59], v[82:83], v[58:59], 0 op_sel_hi:[1,1,0]
	v_lshlrev_b32_e32 v70, 16, v57
	v_and_b32_e32 v71, 0xffff0000, v57
	v_exp_f32_e32 v52, v52
	v_exp_f32_e32 v53, v53
	v_pk_fma_f32 v[58:59], v[86:87], v[70:71], v[58:59]
	v_lshlrev_b32_e32 v70, 16, v69
	v_and_b32_e32 v71, 0xffff0000, v69
	s_waitcnt lgkmcnt(1)
	v_pk_fma_f32 v[58:59], v[98:99], v[70:71], v[58:59]
	v_lshlrev_b32_e32 v70, 16, v73
	v_and_b32_e32 v71, 0xffff0000, v73
	s_waitcnt lgkmcnt(0)
; __device__ __forceinline__ float siluf_(float x) { return x * __builtin_amdgcn_rcpf(1.f + fexp(-x)); }
; __device__ __forceinline__ float lo16(unsigned u) { return __uint_as_float(u << 16); }
; __device__ __forceinline__ float hi16(unsigned u) { return __uint_as_float(u & 0xffff0000u); }
; __device__ void phase_gdn_prep(const Params& p, int l, char* smem, int vb, int nvb, int pend, int oz) {
;     ...
;                 for (int j = 0; j < 4; ++j) {
;                     const u32x4 x0 = *(const u32x4*)(raw + (t + j) * 192 + which * 64 + qt * 16);
;                     const u32x4 x1 = *(const u32x4*)(raw + (t + j) * 192 + which * 64 + qt * 16 + 8);
;                     const float* cwp = cwl + j * 192 + which * 64 + qt * 16;
; #pragma unroll
;                     for (int w = 0; w < 4; ++w) {
;                         a[2 * w] += cwp[2 * w] * lo16(x0[w]);
;                         a[2 * w + 1] += cwp[2 * w + 1] * hi16(x0[w]);
;                         a[8 + 2 * w] += cwp[8 + 2 * w] * lo16(x1[w]);
;                         a[8 + 2 * w + 1] += cwp[8 + 2 * w + 1] * hi16(x1[w]);
;                     }
;                 }
;                 float ss = 0.f;
; #pragma unroll
;                 for (int i = 0; i < 16; ++i) {
;                     a[i] = siluf_(a[i]);
;                     ss += a[i] * a[i];
;                 }
;                 float sc = 1.f;
;                 if (which < 2) {
;                     ss += __shfl_xor(ss, 1);
;                     ss += __shfl_xor(ss, 2);
;                     sc = rsqrtf(ss + EPS) * (which == 0 ? 0.125f : 1.f);
;                 }
	v_pk_fma_f32 v[58:59], v[102:103], v[70:71], v[58:59]
	v_add_f32_e32 v52, 1.0, v52
	v_mul_f32_e32 v51, 0xbfb8aa3b, v58
	v_add_f32_e32 v53, 1.0, v53
	v_exp_f32_e32 v51, v51
	v_rcp_f32_e32 v52, v52
	v_rcp_f32_e32 v53, v53
	v_mul_f32_e32 v57, 0xbfb8aa3b, v59
	v_exp_f32_e32 v57, v57
	v_add_f32_e32 v51, 1.0, v51
	v_lshlrev_b32_e32 v70, 16, v50
	v_and_b32_e32 v71, 0xffff0000, v50
	v_pk_mul_f32 v[42:43], v[42:43], v[52:53]
	v_rcp_f32_e32 v52, v51
	v_pk_fma_f32 v[50:51], v[80:81], v[70:71], 0 op_sel_hi:[1,1,0]
	v_lshlrev_b32_e32 v70, 16, v56
	v_and_b32_e32 v71, 0xffff0000, v56
	v_add_f32_e32 v53, 1.0, v57
	v_pk_fma_f32 v[50:51], v[84:85], v[70:71], v[50:51]
	v_lshlrev_b32_e32 v56, 16, v68
	v_and_b32_e32 v57, 0xffff0000, v68
	v_pk_fma_f32 v[50:51], v[96:97], v[56:57], v[50:51]
	v_lshlrev_b32_e32 v56, 16, v72
	v_and_b32_e32 v57, 0xffff0000, v72
	v_pk_fma_f32 v[68:69], v[100:101], v[56:57], v[50:51]
	v_rcp_f32_e32 v53, v53
	v_mul_f32_e32 v50, 0xbfb8aa3b, v68
	v_exp_f32_e32 v50, v50
	v_mul_f32_e32 v51, 0xbfb8aa3b, v69
	v_exp_f32_e32 v51, v51
	v_pk_mul_f32 v[40:41], v[78:79], v[90:91]
	v_add_f32_e32 v50, 1.0, v50
	v_rcp_f32_e32 v70, v50
	v_add_f32_e32 v50, 1.0, v51
	v_rcp_f32_e32 v71, v50
	v_pk_mul_f32 v[50:51], v[58:59], v[52:53]
	v_lshlrev_b32_e32 v80, 16, v19
	v_and_b32_e32 v81, 0xffff0000, v19
	v_pk_mul_f32 v[52:53], v[68:69], v[70:71]
	ds_read_b128 v[68:71], v61 offset:53648
	ds_read_b128 v[72:75], v61 offset:54416
	ds_read_b128 v[76:79], v61 offset:53632
	v_lshlrev_b32_e32 v84, 16, v15
	v_and_b32_e32 v85, 0xffff0000, v15
	v_rcp_f32_e32 v137, v67
	s_waitcnt lgkmcnt(2)
	v_pk_fma_f32 v[70:71], v[70:71], v[80:81], 0 op_sel_hi:[1,1,0]
	ds_read_b128 v[80:83], v61 offset:54400
	s_waitcnt lgkmcnt(2)
	v_pk_fma_f32 v[70:71], v[74:75], v[84:85], v[70:71]
	ds_read_b128 v[84:87], v61 offset:55184
	ds_read_b128 v[88:91], v61 offset:55952
	ds_read_b128 v[92:95], v61 offset:55168
	v_lshlrev_b32_e32 v74, 16, v11
	v_and_b32_e32 v75, 0xffff0000, v11
	ds_read_b128 v[96:99], v61 offset:55936
	s_waitcnt lgkmcnt(3)
	v_pk_fma_f32 v[70:71], v[86:87], v[74:75], v[70:71]
	v_lshlrev_b32_e32 v74, 16, v7
	v_and_b32_e32 v75, 0xffff0000, v7
	s_waitcnt lgkmcnt(2)
	v_pk_fma_f32 v[70:71], v[90:91], v[74:75], v[70:71]
	v_lshlrev_b32_e32 v90, 16, v18
	v_mul_f32_e32 v7, 0xbfb8aa3b, v70
	v_exp_f32_e32 v7, v7
	v_mul_f32_e32 v11, 0xbfb8aa3b, v71
	v_exp_f32_e32 v11, v11
	v_and_b32_e32 v91, 0xffff0000, v18
	v_pk_fma_f32 v[18:19], v[68:69], v[90:91], 0 op_sel_hi:[1,1,0]
	v_lshlrev_b32_e32 v68, 16, v14
	v_and_b32_e32 v69, 0xffff0000, v14
	v_add_f32_e32 v7, 1.0, v7
	v_pk_fma_f32 v[14:15], v[72:73], v[68:69], v[18:19]
	v_lshlrev_b32_e32 v18, 16, v10
	v_and_b32_e32 v19, 0xffff0000, v10
	v_rcp_f32_e32 v86, v7
	v_add_f32_e32 v7, 1.0, v11
	v_pk_fma_f32 v[10:11], v[84:85], v[18:19], v[14:15]
	v_lshlrev_b32_e32 v18, 16, v17
	v_and_b32_e32 v19, 0xffff0000, v17
	v_pk_fma_f32 v[18:19], v[78:79], v[18:19], 0 op_sel_hi:[1,1,0]
	v_lshlrev_b32_e32 v68, 16, v13
	v_and_b32_e32 v69, 0xffff0000, v13
	v_pk_fma_f32 v[18:19], v[82:83], v[68:69], v[18:19]
	v_lshlrev_b32_e32 v68, 16, v9
	v_and_b32_e32 v69, 0xffff0000, v9
	v_rcp_f32_e32 v87, v7
	s_waitcnt lgkmcnt(1)
	v_pk_fma_f32 v[18:19], v[94:95], v[68:69], v[18:19]
	v_lshlrev_b32_e32 v68, 16, v5
	v_and_b32_e32 v69, 0xffff0000, v5
	s_waitcnt lgkmcnt(0)
	v_pk_fma_f32 v[18:19], v[98:99], v[68:69], v[18:19]
	v_lshlrev_b32_e32 v14, 16, v6
	v_mul_f32_e32 v5, 0xbfb8aa3b, v18
	v_mul_f32_e32 v9, 0xbfb8aa3b, v19
	v_and_b32_e32 v15, 0xffff0000, v6
	v_exp_f32_e32 v5, v5
	v_exp_f32_e32 v9, v9
	v_pk_fma_f32 v[6:7], v[88:89], v[14:15], v[10:11]
	v_pk_mul_f32 v[14:15], v[70:71], v[86:87]
	v_lshlrev_b32_e32 v70, 16, v16
	v_and_b32_e32 v71, 0xffff0000, v16
	v_pk_fma_f32 v[16:17], v[76:77], v[70:71], 0 op_sel_hi:[1,1,0]
	v_lshlrev_b32_e32 v70, 16, v12
	v_and_b32_e32 v71, 0xffff0000, v12
	v_pk_fma_f32 v[12:13], v[80:81], v[70:71], v[16:17]
	v_lshlrev_b32_e32 v16, 16, v8
	v_and_b32_e32 v17, 0xffff0000, v8
	v_add_f32_e32 v5, 1.0, v5
	v_add_f32_e32 v67, 1.0, v9
	v_pk_fma_f32 v[8:9], v[92:93], v[16:17], v[12:13]
	v_lshlrev_b32_e32 v12, 16, v4
	v_and_b32_e32 v13, 0xffff0000, v4
	v_rcp_f32_e32 v68, v5
	v_pk_fma_f32 v[4:5], v[96:97], v[12:13], v[8:9]
	v_mul_f32_e32 v10, 0xbfb8aa3b, v6
	v_mul_f32_e32 v8, 0xbfb8aa3b, v4
	v_mul_f32_e32 v9, 0xbfb8aa3b, v5
	v_exp_f32_e32 v8, v8
	v_exp_f32_e32 v9, v9
	v_mul_f32_e32 v11, 0xbfb8aa3b, v7
	v_exp_f32_e32 v10, v10
	v_exp_f32_e32 v11, v11
	v_add_f32_e32 v8, 1.0, v8
	v_add_f32_e32 v9, 1.0, v9
	v_rcp_f32_e32 v69, v67
	v_rcp_f32_e32 v8, v8
	v_rcp_f32_e32 v9, v9
	v_add_f32_e32 v10, 1.0, v10
	v_add_f32_e32 v11, 1.0, v11
	v_pk_mul_f32 v[46:47], v[48:49], v[132:133]
	v_pk_mul_f32 v[48:49], v[134:135], v[136:137]
	v_rcp_f32_e32 v10, v10
	v_rcp_f32_e32 v11, v11
	v_pk_mul_f32 v[18:19], v[18:19], v[68:69]
	v_pk_mul_f32 v[68:69], v[4:5], v[8:9]
	v_mov_b32_e32 v73, v49
	v_mov_b32_e32 v72, v69
	v_mov_b32_e32 v70, v68
	v_mov_b32_e32 v71, v48
	v_pk_mul_f32 v[72:73], v[72:73], v[72:73]
	v_mov_b32_e32 v8, v18
	v_mov_b32_e32 v9, v46
	v_pk_fma_f32 v[70:71], v[70:71], v[70:71], v[72:73]
	v_pk_mul_f32 v[16:17], v[6:7], v[10:11]
	v_mov_b32_e32 v10, v19
	v_mov_b32_e32 v11, v47
	v_pk_fma_f32 v[8:9], v[8:9], v[8:9], v[70:71]
	v_mov_b32_e32 v4, v16
	v_mov_b32_e32 v5, v44
	v_pk_fma_f32 v[8:9], v[10:11], v[10:11], v[8:9]
	v_pk_mul_f32 v[12:13], v[14:15], v[14:15]
	v_mov_b32_e32 v6, v17
	v_mov_b32_e32 v7, v45
	v_pk_fma_f32 v[4:5], v[4:5], v[4:5], v[8:9]
	v_pk_mul_f32 v[74:75], v[52:53], v[52:53]
	v_pk_fma_f32 v[4:5], v[6:7], v[6:7], v[4:5]
	v_mov_b32_e32 v6, v12
	v_mov_b32_e32 v7, v38
	v_pk_add_f32 v[4:5], v[4:5], v[6:7]
	v_mov_b32_e32 v38, v13
	v_pk_add_f32 v[4:5], v[4:5], v[38:39]
	v_mov_b32_e32 v6, v74
	v_mov_b32_e32 v7, v36
	v_pk_mul_f32 v[34:35], v[26:27], v[26:27]
	v_pk_mul_f32 v[58:59], v[50:51], v[50:51]
	v_pk_add_f32 v[4:5], v[6:7], v[4:5]
	v_mov_b32_e32 v36, v75
	v_pk_add_f32 v[4:5], v[36:37], v[4:5]
	v_mov_b32_e32 v6, v58
	v_mov_b32_e32 v7, v34
	v_pk_mul_f32 v[28:29], v[22:23], v[22:23]
	v_pk_mul_f32 v[56:57], v[42:43], v[42:43]
	v_pk_add_f32 v[4:5], v[6:7], v[4:5]
	v_mov_b32_e32 v34, v59
	v_pk_add_f32 v[4:5], v[34:35], v[4:5]
	v_mov_b32_e32 v6, v56
	v_mov_b32_e32 v7, v28
	v_pk_mul_f32 v[24:25], v[20:21], v[20:21]
	v_pk_mul_f32 v[54:55], v[40:41], v[40:41]
	v_pk_add_f32 v[4:5], v[6:7], v[4:5]
	v_mov_b32_e32 v28, v57
	v_pk_add_f32 v[4:5], v[28:29], v[4:5]
	v_mov_b32_e32 v6, v54
	v_mov_b32_e32 v7, v24
	v_pk_add_f32 v[4:5], v[6:7], v[4:5]
	v_mov_b32_e32 v24, v55
	v_pk_add_f32 v[4:5], v[24:25], v[4:5]
	s_waitcnt lgkmcnt(0)
; __device__ void phase_gdn_prep(const Params& p, int l, char* smem, int vb, int nvb, int pend, int oz) {
;     ...
;                 float sc = 1.f;
;                 if (which < 2) {
;                     ss += __shfl_xor(ss, 1);
;                     ss += __shfl_xor(ss, 2);
;                     sc = rsqrtf(ss + EPS) * (which == 0 ? 0.125f : 1.f);
;                 }
;                 bf16_t* dst = (which == 0 ? qs : which == 1 ? ks : vs) + t * LS + qt * 16;
;                 u32x4 o0 = {cvt_pk(a[0] * sc, a[1] * sc), cvt_pk(a[2] * sc, a[3] * sc), cvt_pk(a[4] * sc, a[5] * sc), cvt_pk(a[6] * sc, a[7] * sc)};
;                 u32x4 o1 = {cvt_pk(a[8] * sc, a[9] * sc), cvt_pk(a[10] * sc, a[11] * sc), cvt_pk(a[12] * sc, a[13] * sc), cvt_pk(a[14] * sc, a[15] * sc)};
;                 *(u32x4*)dst = o0;
;                 *(u32x4*)(dst + 8) = o1;
;             }
	s_nop 1
	v_add_f32_dpp v4, v4, v4 quad_perm:[1,0,3,2] row_mask:0xf bank_mask:0xf
	v_add_f32_dpp v5, v5, v5 quad_perm:[1,0,3,2] row_mask:0xf bank_mask:0xf
	s_mov_b32 s0, 0x358637bd
	s_cmp_gt_i32 s2, 1
	s_nop 1
	v_add_f32_dpp v4, v4, v4 quad_perm:[2,3,0,1] row_mask:0xf bank_mask:0xf
	v_add_f32_dpp v5, v5, v5 quad_perm:[2,3,0,1] row_mask:0xf bank_mask:0xf
	s_nop 0
	v_pk_add_f32 v[12:13], v[4:5], s[0:1] op_sel_hi:[1,0]
	s_movk_i32 s0, 0x90
	v_mul_f32_e32 v4, 0x4b800000, v13
	v_cmp_gt_f32_e32 vcc, s63, v13
	v_mad_u32_u24 v24, v63, s0, v64
	s_nop 0
	v_cndmask_b32_e32 v4, v13, v4, vcc
	v_rsq_f32_e32 v4, v4
	s_nop 0
	v_mul_f32_e32 v5, 0x45800000, v4
	v_cndmask_b32_e32 v4, v4, v5, vcc
	v_mul_f32_e32 v28, 0x3e000000, v4
	v_pk_mul_f32 v[4:5], v[48:49], v[28:29] op_sel_hi:[1,0]
	v_pk_mul_f32 v[6:7], v[46:47], v[28:29] op_sel_hi:[1,0]
	v_cvt_pk_bf16_f32 v4, v4, v5
	v_cvt_pk_bf16_f32 v5, v6, v7
	v_pk_mul_f32 v[6:7], v[44:45], v[28:29] op_sel_hi:[1,0]
	v_pk_mul_f32 v[8:9], v[32:33], v[28:29] op_sel_hi:[1,0]
	v_cvt_pk_bf16_f32 v6, v6, v7
	v_cvt_pk_bf16_f32 v7, v8, v9
	v_pk_mul_f32 v[8:9], v[30:31], v[28:29] op_sel_hi:[1,0]
	v_pk_mul_f32 v[10:11], v[26:27], v[28:29] op_sel_hi:[1,0]
	v_cvt_pk_bf16_f32 v8, v8, v9
	v_cvt_pk_bf16_f32 v9, v10, v11
	v_pk_mul_f32 v[10:11], v[22:23], v[28:29] op_sel_hi:[1,0]
	v_cmp_gt_f32_e32 vcc, s63, v12
	v_cvt_pk_bf16_f32 v10, v10, v11
	v_mul_f32_e32 v11, 0x4b800000, v12
	v_cndmask_b32_e32 v11, v12, v11, vcc
	v_rsq_f32_e32 v12, v11
	v_pk_mul_f32 v[20:21], v[20:21], v[28:29] op_sel_hi:[1,0]
	s_nop 0
	v_cvt_pk_bf16_f32 v11, v20, v21
	ds_write_b128 v24, v[4:7] offset:25728
	ds_write_b128 v24, v[8:11] offset:25744
	v_mul_f32_e32 v4, 0x45800000, v12
	v_cndmask_b32_e32 v12, v12, v4, vcc
	v_pk_mul_f32 v[4:5], v[68:69], v[12:13] op_sel_hi:[1,0]
	v_pk_mul_f32 v[6:7], v[18:19], v[12:13] op_sel_hi:[1,0]
	v_cvt_pk_bf16_f32 v4, v4, v5
	v_cvt_pk_bf16_f32 v5, v6, v7
	v_pk_mul_f32 v[6:7], v[16:17], v[12:13] op_sel_hi:[1,0]
	v_pk_mul_f32 v[8:9], v[14:15], v[12:13] op_sel_hi:[1,0]
	v_cvt_pk_bf16_f32 v6, v6, v7
	v_cvt_pk_bf16_f32 v7, v8, v9
	v_pk_mul_f32 v[8:9], v[52:53], v[12:13] op_sel_hi:[1,0]
	v_pk_mul_f32 v[10:11], v[50:51], v[12:13] op_sel_hi:[1,0]
	v_cvt_pk_bf16_f32 v8, v8, v9
	v_cvt_pk_bf16_f32 v9, v10, v11
	v_pk_mul_f32 v[10:11], v[42:43], v[12:13] op_sel_hi:[1,0]
	v_pk_mul_f32 v[12:13], v[40:41], v[12:13] op_sel_hi:[1,0]
	v_cvt_pk_bf16_f32 v10, v10, v11
	v_cvt_pk_bf16_f32 v11, v12, v13
	ds_write_b128 v24, v[4:7] offset:34944
	ds_write_b128 v24, v[8:11] offset:34960
	ds_read_b128 v[4:7], v62 offset:256
	ds_read_b128 v[26:29], v62 offset:272
	ds_read_b128 v[30:33], v62 offset:656
	ds_read_b128 v[34:37], v61 offset:53920
	ds_read_b128 v[20:23], v61 offset:53936
	ds_read_b128 v[38:41], v62 offset:1040
	ds_read_b128 v[42:45], v62 offset:1424
	s_waitcnt lgkmcnt(5)
	v_lshlrev_b32_e32 v8, 16, v29
	v_and_b32_e32 v9, 0xffff0000, v29
	s_waitcnt lgkmcnt(2)
	v_pk_fma_f32 v[12:13], v[22:23], v[8:9], 0 op_sel_hi:[1,1,0]
	ds_read_b128 v[46:49], v61 offset:54704
	ds_read_b128 v[8:11], v62 offset:640
	v_lshlrev_b32_e32 v14, 16, v33
	v_and_b32_e32 v15, 0xffff0000, v33
	ds_read_b128 v[50:53], v61 offset:54688
	s_waitcnt lgkmcnt(2)
	v_pk_fma_f32 v[16:17], v[48:49], v[14:15], v[12:13]
	ds_read_b128 v[54:57], v61 offset:55472
	ds_read_b128 v[12:15], v62 offset:1024
	v_lshlrev_b32_e32 v18, 16, v41
	v_and_b32_e32 v19, 0xffff0000, v41
	ds_read_b128 v[64:67], v61 offset:55456
	s_waitcnt lgkmcnt(2)
	v_pk_fma_f32 v[22:23], v[56:57], v[18:19], v[16:17]
	ds_read_b128 v[56:59], v61 offset:56240
	ds_read_b128 v[16:19], v62 offset:1408
	v_lshlrev_b32_e32 v48, 16, v45
	v_and_b32_e32 v49, 0xffff0000, v45
	ds_read_b128 v[68:71], v61 offset:56224
	s_waitcnt lgkmcnt(2)
	v_pk_fma_f32 v[22:23], v[58:59], v[48:49], v[22:23]
	v_lshlrev_b32_e32 v58, 16, v28
	v_mul_f32_e32 v25, 0xbfb8aa3b, v23
	v_exp_f32_e32 v25, v25
	v_mul_f32_e32 v29, 0xbfb8aa3b, v22
	v_exp_f32_e32 v29, v29
	v_and_b32_e32 v59, 0xffff0000, v28
	v_add_f32_e32 v25, 1.0, v25
	v_rcp_f32_e32 v49, v25
	v_add_f32_e32 v25, 1.0, v29
	v_pk_fma_f32 v[20:21], v[20:21], v[58:59], 0 op_sel_hi:[1,1,0]
	v_lshlrev_b32_e32 v28, 16, v32
	v_and_b32_e32 v29, 0xffff0000, v32
	v_pk_fma_f32 v[20:21], v[46:47], v[28:29], v[20:21]
	v_lshlrev_b32_e32 v28, 16, v40
	v_and_b32_e32 v29, 0xffff0000, v40
	v_pk_fma_f32 v[20:21], v[54:55], v[28:29], v[20:21]
	v_lshlrev_b32_e32 v28, 16, v44
	v_and_b32_e32 v29, 0xffff0000, v44
	v_pk_fma_f32 v[28:29], v[56:57], v[28:29], v[20:21]
	v_rcp_f32_e32 v48, v25
	v_mul_f32_e32 v20, 0xbfb8aa3b, v29
	v_exp_f32_e32 v25, v20
	v_mul_f32_e32 v20, 0xbfb8aa3b, v28
	v_exp_f32_e32 v32, v20
	v_pk_mul_f32 v[20:21], v[22:23], v[48:49]
	v_add_f32_e32 v22, 1.0, v25
	v_rcp_f32_e32 v23, v22
	v_add_f32_e32 v22, 1.0, v32
	v_lshlrev_b32_e32 v32, 16, v27
	v_and_b32_e32 v33, 0xffff0000, v27
	v_pk_fma_f32 v[32:33], v[36:37], v[32:33], 0 op_sel_hi:[1,1,0]
	v_lshlrev_b32_e32 v36, 16, v31
	v_and_b32_e32 v37, 0xffff0000, v31
	v_pk_fma_f32 v[32:33], v[52:53], v[36:37], v[32:33]
	v_lshlrev_b32_e32 v36, 16, v39
	v_and_b32_e32 v37, 0xffff0000, v39
	v_pk_fma_f32 v[32:33], v[66:67], v[36:37], v[32:33]
	v_lshlrev_b32_e32 v36, 16, v43
	v_and_b32_e32 v37, 0xffff0000, v43
	s_waitcnt lgkmcnt(0)
; __device__ void phase_gdn_prep(const Params& p, int l, char* smem, int vb, int nvb, int pend, int oz) {
;     ...
;             for (int which = 0; which < 3; ++which) {
;                 float a[16];
; #pragma unroll
;                 for (int i = 0; i < 16; ++i) a[i] = 0.f;
; #pragma unroll
;                 for (int j = 0; j < 4; ++j) {
;                     const u32x4 x0 = *(const u32x4*)(raw + (t + j) * 192 + which * 64 + qt * 16);
;                     const u32x4 x1 = *(const u32x4*)(raw + (t + j) * 192 + which * 64 + qt * 16 + 8);
;                     const float* cwp = cwl + j * 192 + which * 64 + qt * 16;
; #pragma unroll
;                     for (int w = 0; w < 4; ++w) {
;                         a[2 * w] += cwp[2 * w] * lo16(x0[w]);
;                         a[2 * w + 1] += cwp[2 * w + 1] * hi16(x0[w]);
;                         a[8 + 2 * w] += cwp[8 + 2 * w] * lo16(x1[w]);
;                         a[8 + 2 * w + 1] += cwp[8 + 2 * w + 1] * hi16(x1[w]);
;                     }
;                 }
;                 float ss = 0.f;
; #pragma unroll
;                 for (int i = 0; i < 16; ++i) {
;                     a[i] = siluf_(a[i]);
;                     ss += a[i] * a[i];
;                 }
;                 float sc = 1.f;
;                 if (which < 2) {
;                     ss += __shfl_xor(ss, 1);
;                     ss += __shfl_xor(ss, 2);
;                     sc = rsqrtf(ss + EPS) * (which == 0 ? 0.125f : 1.f);
;                 }
;                 bf16_t* dst = (which == 0 ? qs : which == 1 ? ks : vs) + t * LS + qt * 16;
;                 u32x4 o0 = {cvt_pk(a[0] * sc, a[1] * sc), cvt_pk(a[2] * sc, a[3] * sc), cvt_pk(a[4] * sc, a[5] * sc), cvt_pk(a[6] * sc, a[7] * sc)};
;                 u32x4 o1 = {cvt_pk(a[8] * sc, a[9] * sc), cvt_pk(a[10] * sc, a[11] * sc), cvt_pk(a[12] * sc, a[13] * sc), cvt_pk(a[14] * sc, a[15] * sc)};
;                 *(u32x4*)dst = o0;
;                 *(u32x4*)(dst + 8) = o1;
;             }
;         }
;         if (wave < 2) {
;             float v = gl[wave * 64 + lane];
; #pragma unroll
;             for (int off = 1; off < 64; off <<= 1) {
;                 const float nb = wave == 0 ? __shfl_up(v, off) : __shfl_down(v, off);
;                 const bool ok = wave == 0 ? (lane >= off) : (lane + off < 64);
;                 v += ok ? nb : 0.f;
;             }
;             Gl[wave * 64 + lane] = v;
	v_pk_fma_f32 v[32:33], v[70:71], v[36:37], v[32:33]
	v_rcp_f32_e32 v22, v22
	v_mul_f32_e32 v25, 0xbfb8aa3b, v33
	v_exp_f32_e32 v25, v25
	v_mul_f32_e32 v27, 0xbfb8aa3b, v32
	v_exp_f32_e32 v27, v27
	v_lshlrev_b32_e32 v36, 16, v26
	v_add_f32_e32 v25, 1.0, v25
	v_and_b32_e32 v37, 0xffff0000, v26
	v_pk_mul_f32 v[22:23], v[28:29], v[22:23]
	v_rcp_f32_e32 v29, v25
	v_add_f32_e32 v25, 1.0, v27
	v_pk_fma_f32 v[26:27], v[34:35], v[36:37], 0 op_sel_hi:[1,1,0]
	v_lshlrev_b32_e32 v34, 16, v30
	v_and_b32_e32 v35, 0xffff0000, v30
	v_pk_fma_f32 v[26:27], v[50:51], v[34:35], v[26:27]
	v_lshlrev_b32_e32 v30, 16, v38
	v_and_b32_e32 v31, 0xffff0000, v38
	v_pk_fma_f32 v[26:27], v[64:65], v[30:31], v[26:27]
	v_lshlrev_b32_e32 v30, 16, v42
	v_and_b32_e32 v31, 0xffff0000, v42
	v_pk_fma_f32 v[50:51], v[68:69], v[30:31], v[26:27]
	v_rcp_f32_e32 v28, v25
	v_mul_f32_e32 v25, 0xbfb8aa3b, v51
	v_exp_f32_e32 v25, v25
	v_mul_f32_e32 v26, 0xbfb8aa3b, v50
	v_exp_f32_e32 v26, v26
	ds_read_b128 v[72:75], v61 offset:53888
	ds_read_b128 v[76:79], v61 offset:53904
	v_add_f32_e32 v25, 1.0, v25
	v_pk_mul_f32 v[52:53], v[32:33], v[28:29]
	v_rcp_f32_e32 v55, v25
	v_add_f32_e32 v25, 1.0, v26
	ds_read_b128 v[26:29], v61 offset:54672
	v_lshlrev_b32_e32 v30, 16, v7
	v_and_b32_e32 v31, 0xffff0000, v7
	s_waitcnt lgkmcnt(1)
	v_pk_fma_f32 v[34:35], v[78:79], v[30:31], 0 op_sel_hi:[1,1,0]
	v_lshlrev_b32_e32 v36, 16, v11
	v_and_b32_e32 v37, 0xffff0000, v11
	ds_read_b128 v[30:33], v61 offset:54656
	s_waitcnt lgkmcnt(1)
	v_pk_fma_f32 v[28:29], v[28:29], v[36:37], v[34:35]
	ds_read_b128 v[34:37], v61 offset:55440
	ds_read_b128 v[38:41], v61 offset:56208
	ds_read_b128 v[42:45], v61 offset:55424
	v_lshlrev_b32_e32 v46, 16, v15
	v_and_b32_e32 v47, 0xffff0000, v15
	v_rcp_f32_e32 v54, v25
	s_waitcnt lgkmcnt(2)
	v_pk_fma_f32 v[28:29], v[36:37], v[46:47], v[28:29]
	v_lshlrev_b32_e32 v36, 16, v19
	v_and_b32_e32 v37, 0xffff0000, v19
	s_waitcnt lgkmcnt(1)
	v_pk_fma_f32 v[28:29], v[40:41], v[36:37], v[28:29]
	v_lshlrev_b32_e32 v40, 16, v6
	v_mul_f32_e32 v11, 0xbfb8aa3b, v28
	v_exp_f32_e32 v11, v11
	v_and_b32_e32 v41, 0xffff0000, v6
	v_pk_mul_f32 v[36:37], v[50:51], v[54:55]
	v_pk_fma_f32 v[40:41], v[76:77], v[40:41], 0 op_sel_hi:[1,1,0]
	v_lshlrev_b32_e32 v50, 16, v10
	v_and_b32_e32 v51, 0xffff0000, v10
	v_add_f32_e32 v19, 1.0, v11
	v_pk_fma_f32 v[10:11], v[26:27], v[50:51], v[40:41]
	v_lshlrev_b32_e32 v26, 16, v14
	v_and_b32_e32 v27, 0xffff0000, v14
	v_pk_fma_f32 v[10:11], v[34:35], v[26:27], v[10:11]
	v_lshlrev_b32_e32 v14, 16, v18
	v_and_b32_e32 v15, 0xffff0000, v18
	v_pk_fma_f32 v[10:11], v[38:39], v[14:15], v[10:11]
	ds_read_b128 v[46:49], v61 offset:56192
	v_mul_f32_e32 v6, 0xbfb8aa3b, v11
	v_exp_f32_e32 v14, v6
	v_mul_f32_e32 v6, 0xbfb8aa3b, v10
	v_exp_f32_e32 v18, v6
	v_rcp_f32_e32 v6, v19
	v_add_f32_e32 v14, 1.0, v14
	v_rcp_f32_e32 v15, v14
	v_add_f32_e32 v14, 1.0, v18
	v_lshlrev_b32_e32 v18, 16, v5
	v_and_b32_e32 v19, 0xffff0000, v5
	v_pk_fma_f32 v[18:19], v[74:75], v[18:19], 0 op_sel_hi:[1,1,0]
	v_lshlrev_b32_e32 v26, 16, v9
	v_and_b32_e32 v27, 0xffff0000, v9
	v_pk_fma_f32 v[18:19], v[32:33], v[26:27], v[18:19]
	v_lshlrev_b32_e32 v26, 16, v13
	v_and_b32_e32 v27, 0xffff0000, v13
	s_waitcnt lgkmcnt(1)
	v_pk_fma_f32 v[18:19], v[44:45], v[26:27], v[18:19]
	v_lshlrev_b32_e32 v26, 16, v17
	v_and_b32_e32 v27, 0xffff0000, v17
	s_waitcnt lgkmcnt(0)
	v_pk_fma_f32 v[18:19], v[48:49], v[26:27], v[18:19]
	v_lshlrev_b32_e32 v26, 16, v4
	v_mul_f32_e32 v9, 0xbfb8aa3b, v18
	v_exp_f32_e32 v9, v9
	v_and_b32_e32 v27, 0xffff0000, v4
	v_pk_fma_f32 v[26:27], v[72:73], v[26:27], 0 op_sel_hi:[1,1,0]
	v_lshlrev_b32_e32 v32, 16, v8
	v_and_b32_e32 v33, 0xffff0000, v8
	v_add_f32_e32 v17, 1.0, v9
	v_pk_fma_f32 v[8:9], v[30:31], v[32:33], v[26:27]
	v_lshlrev_b32_e32 v26, 16, v12
	v_and_b32_e32 v27, 0xffff0000, v12
	v_pk_fma_f32 v[8:9], v[42:43], v[26:27], v[8:9]
	v_lshlrev_b32_e32 v12, 16, v16
	v_and_b32_e32 v13, 0xffff0000, v16
	v_pk_fma_f32 v[8:9], v[46:47], v[12:13], v[8:9]
	v_mul_f32_e32 v7, 0xbfb8aa3b, v29
	v_mul_f32_e32 v4, 0xbfb8aa3b, v9
	v_mul_f32_e32 v5, 0xbfb8aa3b, v19
	v_exp_f32_e32 v12, v4
	v_mul_f32_e32 v4, 0xbfb8aa3b, v8
	v_exp_f32_e32 v7, v7
	v_exp_f32_e32 v5, v5
	v_exp_f32_e32 v16, v4
	v_add_f32_e32 v12, 1.0, v12
	v_add_f32_e32 v7, 1.0, v7
	v_add_f32_e32 v5, 1.0, v5
	v_rcp_f32_e32 v13, v12
	v_add_f32_e32 v12, 1.0, v16
	v_rcp_f32_e32 v7, v7
	v_rcp_f32_e32 v14, v14
	v_rcp_f32_e32 v5, v5
	v_rcp_f32_e32 v4, v17
	v_rcp_f32_e32 v12, v12
	v_pk_mul_f32 v[16:17], v[28:29], v[6:7]
	v_pk_mul_f32 v[6:7], v[10:11], v[14:15]
	v_pk_mul_f32 v[10:11], v[18:19], v[4:5]
	v_pk_mul_f32 v[4:5], v[8:9], v[12:13]
	v_cvt_pk_bf16_f32 v6, v6, v7
	v_cvt_pk_bf16_f32 v4, v4, v5
	v_cvt_pk_bf16_f32 v5, v10, v11
	v_cvt_pk_bf16_f32 v7, v16, v17
	v_cvt_pk_bf16_f32 v8, v36, v37
	v_cvt_pk_bf16_f32 v9, v52, v53
	v_cvt_pk_bf16_f32 v10, v22, v23
	v_cvt_pk_bf16_f32 v11, v20, v21
	ds_write_b128 v24, v[4:7] offset:44160
	ds_write_b128 v24, v[8:11] offset:44176
	s_cbranch_scc1 .LBB0_549
	v_lshlrev_b32_e32 v4, 2, v60
	v_lshl_or_b32 v4, s2, 8, v4
	v_add_u32_e32 v4, s81, v4
	ds_read_b32 v5, v4 offset:56448
	s_waitcnt lgkmcnt(0)
	v_mov_b32_e32 v6, v5
	s_nop 1
	v_add_f32_dpp v6, v5, v6 row_shr:1 row_mask:0xf bank_mask:0xf
	v_add_f32_dpp v6, v5, v6 row_shr:2 row_mask:0xf bank_mask:0xf
	v_add_f32_dpp v6, v5, v6 row_shr:3 row_mask:0xf bank_mask:0xf
	s_nop 1
	v_add_f32_dpp v6, v6, v6 row_shr:4 row_mask:0xf bank_mask:0xe
	s_nop 1
	v_add_f32_dpp v6, v6, v6 row_shr:8 row_mask:0xf bank_mask:0xc
	s_nop 1
	v_add_f32_dpp v6, v6, v6 row_bcast:15 row_mask:0xa bank_mask:0xf
	s_nop 1
	v_add_f32_dpp v6, v6, v6 row_bcast:31 row_mask:0xc bank_mask:0xf
	s_cmp_eq_u32 s2, 0
	s_cbranch_scc1 .Lgp_cs_fwd
	s_nop 0
	v_readlane_b32 s0, v6, 63
	s_nop 1
	v_sub_f32_e32 v6, s0, v6
	v_add_f32_e32 v6, v5, v6
